# scan loop: S *= gl back to 32 packed multiplies (fewer issue slots), otherwise as v26
# speedup vs baseline: 1.0040x; 1.0040x over previous
; DI float bflo(unsigned u) { return __uint_as_float(u << 16); }
; DI float bfhi(unsigned u) { return __uint_as_float(u & 0xffff0000u); }
; DI bf16x8 packS(const f32x16& x, int s) { return pack8(x[8 * s], x[8 * s + 1], x[8 * s + 2], x[8 * s + 3], x[8 * s + 4], x[8 * s + 5], x[8 * s + 6], x[8 * s + 7]); }
; #define SCAN_RDW(F, mh) do { _Pragma("unroll") for (int k = 0; k < 8; ++k) { const int i2 = k >> 2, m = 2 * (mh) + ((k >> 1) & 1), sx = k & 1; F[k] = *(const bf16x8*)(lw + ((i2 * 4 + m) * 2 + sx) * 1024); } } while (0)
; DI void gdn_scan_seq(const Params& p, int bh16, char* ldsf) {
;     ...
;     char* sco = scp + (size_t)c * 32768;
;     bf16x8 Sb[4][2];
; #pragma unroll
;     for (int m = 0; m < 4; ++m) { Sb[m][0] = packS(S[m], 0); Sb[m][1] = packS(S[m], 1); *(bf16x8*)(sco + (m * 2 + 0) * 1024) = Sb[m][0]; *(bf16x8*)(sco + (m * 2 + 1) * 1024) = Sb[m][1]; }
;     __builtin_amdgcn_sched_barrier(0);
;     if (c + 2 < 128) { const int s2 = sl >= 1 ? sl - 1 : 2; SCAN_ISSUE(c + 2, s2); }
;     const char* base = ldsf + sl * 49152;
;     const char* lw = base + lane * 16; const char* lk = lw + 16384; const char* lu = base + 32768 + wv * 4096 + lane * 16;
;     const float gl = glt[c];
;     f32x16 vn[2];
; #pragma unroll
;     for (int i2 = 0; i2 < 2; ++i2) {
;       const u32x4 ua = *(const u32x4*)(lu + (2 * i2) * 1024), ub = *(const u32x4*)(lu + (2 * i2 + 1) * 1024);
; #pragma unroll
;       for (int e = 0; e < 4; ++e) { vn[i2][2 * e] = bflo(ua[e]); vn[i2][2 * e + 1] = bfhi(ua[e]); vn[i2][8 + 2 * e] = bflo(ub[e]); vn[i2][8 + 2 * e + 1] = bfhi(ub[e]); }
;     }
;     bf16x8 fa[8], fb[8];
;     ...
;     SCAN_RDW(fa, 0);
;     __builtin_amdgcn_sched_barrier(0);
;     SCAN_RDW(fb, 1);
;     __builtin_amdgcn_sched_barrier(0);
;     SCAN_MMW(fa, 0);
;     __builtin_amdgcn_sched_barrier(0);
;     SCAN_RDK(fa, 0);
;     __builtin_amdgcn_sched_barrier(0);
;     SCAN_MMW(fb, 1);
;     __builtin_amdgcn_sched_barrier(0);
;     SCAN_RDK(fb, 1);
;     __builtin_amdgcn_sched_barrier(0);
;     bf16x8 Vb[2][2];
; #pragma unroll
;     for (int j2 = 0; j2 < 2; ++j2) { Vb[j2][0] = packS(vn[j2], 0); Vb[j2][1] = packS(vn[j2], 1); }
; #pragma unroll
;     for (int m = 0; m < 4; ++m)
; #pragma unroll
;       for (int r = 0; r < 16; ++r) S[m][r] *= gl;
.Lscan_noprog:
	v_add_u32_e32 v131, s3, v130
	v_add_u32_e32 v134, s3, v129
	v_mov_b32_e32 v143, s18
	ds_read_b128 v[72:75], v134 offset:32768
	ds_read_b128 v[76:79], v134 offset:33792
	ds_read_b32 v142, v143
	ds_read_b128 v[148:151], v131 offset:0
	ds_read_b128 v[152:155], v131 offset:1024
	ds_read_b128 v[156:159], v131 offset:2048
	ds_read_b128 v[160:163], v131 offset:3072
	ds_read_b128 v[164:167], v131 offset:4096
	ds_read_b128 v[168:171], v131 offset:5120
	ds_read_b128 v[172:175], v131 offset:6144
	ds_read_b128 v[178:181], v131 offset:7168
	ds_read_b128 v[88:91], v134 offset:34816
	ds_read_b128 v[92:95], v134 offset:35840
	s_waitcnt lgkmcnt(10)
	v_mfma_f32_32x32x16_bf16 v[0:15], v[182:185], v[80:83], v[0:15]
	v_lshlrev_b32_e32 v64, 16, v72
	v_and_b32_e32 v65, 0xffff0000, v72
	v_lshlrev_b32_e32 v66, 16, v73
	v_and_b32_e32 v67, 0xffff0000, v73
	v_mfma_f32_32x32x16_bf16 v[0:15], v[190:193], v[84:87], v[0:15]
	v_lshlrev_b32_e32 v68, 16, v74
	v_and_b32_e32 v69, 0xffff0000, v74
	v_lshlrev_b32_e32 v70, 16, v75
	v_and_b32_e32 v71, 0xffff0000, v75
	v_mfma_f32_32x32x16_bf16 v[16:31], v[194:197], v[80:83], v[16:31]
	v_lshlrev_b32_e32 v72, 16, v76
	v_and_b32_e32 v73, 0xffff0000, v76
	v_lshlrev_b32_e32 v74, 16, v77
	v_and_b32_e32 v75, 0xffff0000, v77
	v_mfma_f32_32x32x16_bf16 v[16:31], v[198:201], v[84:87], v[16:31]
	v_lshlrev_b32_e32 v76, 16, v78
	v_and_b32_e32 v77, 0xffff0000, v78
	v_lshlrev_b32_e32 v78, 16, v79
	v_and_b32_e32 v79, 0xffff0000, v79
	s_waitcnt lgkmcnt(8)
	ds_read_b128 v[182:185], v131 offset:8192
	ds_read_b128 v[190:193], v131 offset:9216
	ds_read_b128 v[194:197], v131 offset:10240
	ds_read_b128 v[198:201], v131 offset:11264
	v_mfma_f32_32x32x16_bf16 v[32:47], v[202:205], v[80:83], v[32:47]
	v_cvt_pk_bf16_f32 v96, v0, v1
	v_cvt_pk_bf16_f32 v97, v2, v3
	v_cvt_pk_bf16_f32 v98, v4, v5
	v_cvt_pk_bf16_f32 v99, v6, v7
	v_cvt_pk_bf16_f32 v100, v8, v9
	v_mfma_f32_32x32x16_bf16 v[32:47], v[208:211], v[84:87], v[32:47]
	v_cvt_pk_bf16_f32 v101, v10, v11
	v_cvt_pk_bf16_f32 v102, v12, v13
	v_cvt_pk_bf16_f32 v103, v14, v15
	v_mfma_f32_32x32x16_bf16 v[48:63], v[212:215], v[80:83], v[48:63]
	v_cvt_pk_bf16_f32 v104, v16, v17
	v_cvt_pk_bf16_f32 v105, v18, v19
	v_cvt_pk_bf16_f32 v106, v20, v21
	v_cvt_pk_bf16_f32 v107, v22, v23
	v_cvt_pk_bf16_f32 v108, v24, v25
	v_mfma_f32_32x32x16_bf16 v[48:63], v[216:219], v[84:87], v[48:63]
	v_cvt_pk_bf16_f32 v109, v26, v27
	v_cvt_pk_bf16_f32 v110, v28, v29
	v_cvt_pk_bf16_f32 v111, v30, v31
	s_waitcnt lgkmcnt(4)
	ds_read_b128 v[202:205], v131 offset:12288
	ds_read_b128 v[208:211], v131 offset:13312
	ds_read_b128 v[212:215], v131 offset:14336
	ds_read_b128 v[216:219], v131 offset:15360
	v_mfma_f32_32x32x16_bf16 v[64:79], v[148:151], v[96:99], v[64:79]
	v_cvt_pk_bf16_f32 v112, v32, v33
	v_cvt_pk_bf16_f32 v113, v34, v35
	v_cvt_pk_bf16_f32 v114, v36, v37
	v_cvt_pk_bf16_f32 v115, v38, v39
	v_lshlrev_b32_e32 v80, 16, v88
	v_mfma_f32_32x32x16_bf16 v[64:79], v[152:155], v[100:103], v[64:79]
	v_cvt_pk_bf16_f32 v116, v40, v41
	v_cvt_pk_bf16_f32 v117, v42, v43
	v_cvt_pk_bf16_f32 v118, v44, v45
	v_cvt_pk_bf16_f32 v119, v46, v47
	v_and_b32_e32 v81, 0xffff0000, v88
	v_mfma_f32_32x32x16_bf16 v[64:79], v[156:159], v[104:107], v[64:79]
	v_cvt_pk_bf16_f32 v120, v48, v49
	v_cvt_pk_bf16_f32 v121, v50, v51
	v_cvt_pk_bf16_f32 v122, v52, v53
	v_cvt_pk_bf16_f32 v123, v54, v55
	v_lshlrev_b32_e32 v82, 16, v89
	v_mfma_f32_32x32x16_bf16 v[64:79], v[160:163], v[108:111], v[64:79]
	v_cvt_pk_bf16_f32 v124, v56, v57
	v_cvt_pk_bf16_f32 v125, v58, v59
	v_cvt_pk_bf16_f32 v126, v60, v61
	v_cvt_pk_bf16_f32 v127, v62, v63
	v_and_b32_e32 v83, 0xffff0000, v89
	ds_read_b128 v[148:151], v131 offset:16384
	ds_read_b128 v[152:155], v131 offset:17408
	ds_read_b128 v[156:159], v131 offset:20480
	ds_read_b128 v[160:163], v131 offset:21504
	v_mfma_f32_32x32x16_bf16 v[64:79], v[164:167], v[112:115], v[64:79]
	v_lshlrev_b32_e32 v84, 16, v90
	v_and_b32_e32 v85, 0xffff0000, v90
	v_lshlrev_b32_e32 v86, 16, v91
	v_and_b32_e32 v87, 0xffff0000, v91
	v_lshlrev_b32_e32 v88, 16, v92
	global_store_dwordx4 v128, v[96:99], s[8:9]
	v_mfma_f32_32x32x16_bf16 v[64:79], v[168:171], v[116:119], v[64:79]
	v_and_b32_e32 v89, 0xffff0000, v92
	v_lshlrev_b32_e32 v90, 16, v93
	v_and_b32_e32 v91, 0xffff0000, v93
	v_lshlrev_b32_e32 v92, 16, v94
	v_and_b32_e32 v93, 0xffff0000, v94
	global_store_dwordx4 v128, v[100:103], s[8:9] offset:1024
	v_mfma_f32_32x32x16_bf16 v[64:79], v[172:175], v[120:123], v[64:79]
	v_lshlrev_b32_e32 v94, 16, v95
	v_and_b32_e32 v95, 0xffff0000, v95
	global_store_dwordx4 v128, v[104:107], s[8:9] offset:2048
	global_store_dwordx4 v128, v[108:111], s[8:9] offset:3072
	v_pk_mul_f32 v[0:1], v[0:1], v[142:143] op_sel_hi:[1,0]
	v_mfma_f32_32x32x16_bf16 v[64:79], v[178:181], v[124:127], v[64:79]
	v_pk_mul_f32 v[2:3], v[2:3], v[142:143] op_sel_hi:[1,0]
	v_pk_mul_f32 v[4:5], v[4:5], v[142:143] op_sel_hi:[1,0]
	v_pk_mul_f32 v[6:7], v[6:7], v[142:143] op_sel_hi:[1,0]
	v_pk_mul_f32 v[8:9], v[8:9], v[142:143] op_sel_hi:[1,0]
	v_pk_mul_f32 v[10:11], v[10:11], v[142:143] op_sel_hi:[1,0]
	s_waitcnt lgkmcnt(8)
; DI bf16x8 packS(const f32x16& x, int s) { return pack8(x[8 * s], x[8 * s + 1], x[8 * s + 2], x[8 * s + 3], x[8 * s + 4], x[8 * s + 5], x[8 * s + 6], x[8 * s + 7]); }
; #define SCAN_MMK(F, mh) do { _Pragma("unroll") for (int q = 0; q < 4; ++q) { const int j2 = q >> 1, sx = q & 1; S[2 * (mh)] = MFMA32(F[q], Vb[j2][sx], S[2 * (mh)]); S[2 * (mh) + 1] = MFMA32(F[4 + q], Vb[j2][sx], S[2 * (mh) + 1]); } } while (0)
; DI void gdn_scan_seq(const Params& p, int bh16, char* ldsf) {
;     ...
;     bf16x8 Vb[2][2];
; #pragma unroll
;     for (int j2 = 0; j2 < 2; ++j2) { Vb[j2][0] = packS(vn[j2], 0); Vb[j2][1] = packS(vn[j2], 1); }
; #pragma unroll
;     for (int m = 0; m < 4; ++m)
; #pragma unroll
;       for (int r = 0; r < 16; ++r) S[m][r] *= gl;
;     SCAN_MMK(fa, 0);
;     SCAN_MMK(fb, 1);
;     ...
;     asm volatile("s_waitcnt lgkmcnt(0)" ::: "memory");
;     sl = sl == 2 ? 0 : sl + 1;
;   }
	ds_read_b128 v[164:167], v131 offset:24576
	ds_read_b128 v[168:171], v131 offset:25600
	ds_read_b128 v[172:175], v131 offset:28672
	ds_read_b128 v[178:181], v131 offset:29696
	v_mfma_f32_32x32x16_bf16 v[80:95], v[182:185], v[96:99], v[80:95]
	v_pk_mul_f32 v[12:13], v[12:13], v[142:143] op_sel_hi:[1,0]
	v_pk_mul_f32 v[14:15], v[14:15], v[142:143] op_sel_hi:[1,0]
	v_pk_mul_f32 v[16:17], v[16:17], v[142:143] op_sel_hi:[1,0]
	v_pk_mul_f32 v[18:19], v[18:19], v[142:143] op_sel_hi:[1,0]
	global_store_dwordx4 v128, v[112:115], s[10:11]
	v_mfma_f32_32x32x16_bf16 v[80:95], v[190:193], v[100:103], v[80:95]
	v_pk_mul_f32 v[20:21], v[20:21], v[142:143] op_sel_hi:[1,0]
	v_pk_mul_f32 v[22:23], v[22:23], v[142:143] op_sel_hi:[1,0]
	v_pk_mul_f32 v[24:25], v[24:25], v[142:143] op_sel_hi:[1,0]
	v_pk_mul_f32 v[26:27], v[26:27], v[142:143] op_sel_hi:[1,0]
	global_store_dwordx4 v128, v[116:119], s[10:11] offset:1024
	v_mfma_f32_32x32x16_bf16 v[80:95], v[194:197], v[104:107], v[80:95]
	v_pk_mul_f32 v[28:29], v[28:29], v[142:143] op_sel_hi:[1,0]
	v_pk_mul_f32 v[30:31], v[30:31], v[142:143] op_sel_hi:[1,0]
	global_store_dwordx4 v128, v[120:123], s[10:11] offset:2048
	global_store_dwordx4 v128, v[124:127], s[10:11] offset:3072
	v_cvt_pk_bf16_f32 v64, v64, v65
	v_pk_mul_f32 v[32:33], v[32:33], v[142:143] op_sel_hi:[1,0]
	v_mfma_f32_32x32x16_bf16 v[80:95], v[198:201], v[108:111], v[80:95]
	v_cvt_pk_bf16_f32 v65, v66, v67
	v_cvt_pk_bf16_f32 v66, v68, v69
	v_cvt_pk_bf16_f32 v67, v70, v71
	v_cvt_pk_bf16_f32 v68, v72, v73
	v_cvt_pk_bf16_f32 v69, v74, v75
	v_pk_mul_f32 v[34:35], v[34:35], v[142:143] op_sel_hi:[1,0]
	s_waitcnt lgkmcnt(8)
	ds_read_b128 v[182:185], v131 offset:18432
	ds_read_b128 v[190:193], v131 offset:19456
	ds_read_b128 v[194:197], v131 offset:22528
	ds_read_b128 v[198:201], v131 offset:23552
	v_mfma_f32_32x32x16_bf16 v[80:95], v[202:205], v[112:115], v[80:95]
	v_cvt_pk_bf16_f32 v70, v76, v77
	v_cvt_pk_bf16_f32 v71, v78, v79
	v_pk_mul_f32 v[36:37], v[36:37], v[142:143] op_sel_hi:[1,0]
	v_pk_mul_f32 v[38:39], v[38:39], v[142:143] op_sel_hi:[1,0]
	v_pk_mul_f32 v[40:41], v[40:41], v[142:143] op_sel_hi:[1,0]
	v_pk_mul_f32 v[42:43], v[42:43], v[142:143] op_sel_hi:[1,0]
	v_mfma_f32_32x32x16_bf16 v[80:95], v[208:211], v[116:119], v[80:95]
	v_pk_mul_f32 v[44:45], v[44:45], v[142:143] op_sel_hi:[1,0]
	v_pk_mul_f32 v[46:47], v[46:47], v[142:143] op_sel_hi:[1,0]
	v_mfma_f32_32x32x16_bf16 v[80:95], v[212:215], v[120:123], v[80:95]
	v_pk_mul_f32 v[48:49], v[48:49], v[142:143] op_sel_hi:[1,0]
	v_pk_mul_f32 v[50:51], v[50:51], v[142:143] op_sel_hi:[1,0]
	v_pk_mul_f32 v[52:53], v[52:53], v[142:143] op_sel_hi:[1,0]
	v_pk_mul_f32 v[54:55], v[54:55], v[142:143] op_sel_hi:[1,0]
	v_pk_mul_f32 v[56:57], v[56:57], v[142:143] op_sel_hi:[1,0]
	v_pk_mul_f32 v[58:59], v[58:59], v[142:143] op_sel_hi:[1,0]
	v_mfma_f32_32x32x16_bf16 v[80:95], v[216:219], v[124:127], v[80:95]
	v_pk_mul_f32 v[60:61], v[60:61], v[142:143] op_sel_hi:[1,0]
	v_pk_mul_f32 v[62:63], v[62:63], v[142:143] op_sel_hi:[1,0]
	s_waitcnt lgkmcnt(8)
	ds_read_b128 v[202:205], v131 offset:26624
	ds_read_b128 v[208:211], v131 offset:27648
	ds_read_b128 v[212:215], v131 offset:30720
	ds_read_b128 v[216:219], v131 offset:31744
	v_mfma_f32_32x32x16_bf16 v[0:15], v[148:151], v[64:67], v[0:15]
	s_add_u32 s2, s2, 1
	s_xor_b32 s3, s3, 0xc000
	s_add_u32 s18, s18, 4
	s_add_u32 s8, s8, 0x8000
	s_addc_u32 s9, s9, 0
	s_add_u32 s10, s10, 0x8000
	s_addc_u32 s11, s11, 0
	v_mfma_f32_32x32x16_bf16 v[0:15], v[152:155], v[68:71], v[0:15]
	v_mfma_f32_32x32x16_bf16 v[16:31], v[156:159], v[64:67], v[16:31]
	v_cvt_pk_bf16_f32 v80, v80, v81
	v_cvt_pk_bf16_f32 v81, v82, v83
	v_cvt_pk_bf16_f32 v82, v84, v85
	v_cvt_pk_bf16_f32 v83, v86, v87
	v_cvt_pk_bf16_f32 v84, v88, v89
	v_cvt_pk_bf16_f32 v85, v90, v91
	v_mfma_f32_32x32x16_bf16 v[16:31], v[160:163], v[68:71], v[16:31]
	v_cvt_pk_bf16_f32 v86, v92, v93
	v_cvt_pk_bf16_f32 v87, v94, v95
	s_waitcnt lgkmcnt(8)
	v_mfma_f32_32x32x16_bf16 v[32:47], v[164:167], v[64:67], v[32:47]
	v_mfma_f32_32x32x16_bf16 v[32:47], v[168:171], v[68:71], v[32:47]
	v_mfma_f32_32x32x16_bf16 v[48:63], v[172:175], v[64:67], v[48:63]
	v_mfma_f32_32x32x16_bf16 v[48:63], v[178:181], v[68:71], v[48:63]
	s_cmp_lt_u32 s2, 0x80
	s_waitcnt lgkmcnt(0)
	s_cbranch_scc1 .Lscan_loop
	s_branch .Lscan_end
